# norm2 row loops (dense and MoE): four scratch loads touch the row after next right after the real next-row loads so the following iteration's loads hit L2 (bottom vmcnt waits +4)
# speedup vs baseline: 1.0070x; 1.0009x over previous
.LBB0_948:
	s_add_u32 s36, s36, s42
	s_addc_u32 s37, s37, s43
	v_readlane_b32 s4, v254, 32
	v_readlane_b32 s5, v254, 33
	s_add_u32 s38, s38, s4
	s_addc_u32 s39, s39, s5
	v_lshl_add_u64 v[152:153], v[152:153], 0, s[78:79]
	s_andn2_b64 vcc, exec, s[70:71]
	s_waitcnt vmcnt(11)
	v_mov_b64_e32 v[170:171], v[156:157]
	s_waitcnt vmcnt(10)
	v_mov_b64_e32 v[168:169], v[158:159]
	s_waitcnt vmcnt(9)
	v_mov_b64_e32 v[166:167], v[160:161]
	s_waitcnt vmcnt(8)
	v_mov_b64_e32 v[164:165], v[162:163]
	s_mov_b32 s40, s33
	s_cbranch_vccz .LBB0_1014
.LBB0_949:
	s_add_i32 s33, s40, s42
	s_cmpk_gt_i32 s33, 0x7fff
	s_cselect_b64 s[70:71], -1, 0
	s_and_b64 vcc, exec, s[70:71]
	s_cbranch_vccnz .LBB0_951
	v_lshl_add_u64 v[156:157], s[6:7], 0, v[152:153]
	v_add_co_u32_e32 v162, vcc, 0x1c00000, v156
	s_nop 1
	v_addc_co_u32_e32 v163, vcc, 0, v157, vcc
	v_lshl_add_u64 v[210:211], v[162:163], 0, s[78:79]
	global_load_dwordx2 v[156:157], v[162:163], off
	global_load_dwordx2 v[158:159], v[162:163], off offset:512
	global_load_dwordx2 v[160:161], v[162:163], off offset:1024
	s_nop 0
	global_load_dwordx2 v[162:163], v[162:163], off offset:1536
	global_load_dwordx2 v[212:213], v[210:211], off
	global_load_dwordx2 v[212:213], v[210:211], off offset:512
	global_load_dwordx2 v[212:213], v[210:211], off offset:1024
	global_load_dwordx2 v[212:213], v[210:211], off offset:1536

.LBB0_1018:
	s_or_b64 exec, exec, s[14:15]
	v_div_scale_f32 v54, s[4:5], v0, v0, s73
	v_rcp_f32_e32 v55, v54
	v_div_scale_f32 v56, vcc, s73, v0, s73
	s_add_u32 s12, s12, s42
	v_fma_f32 v57, -v54, v55, 1.0
	v_fmac_f32_e32 v55, v57, v55
	v_mul_f32_e32 v57, v56, v55
	v_fma_f32 v58, -v54, v57, v56
	v_fmac_f32_e32 v57, v58, v55
	v_fma_f32 v54, -v54, v57, v56
	v_div_fmas_f32 v54, v54, v55, v57
	v_div_fixup_f32 v0, v54, v0, s73
	v_mul_f32_e32 v45, v45, v0
	v_mul_f32_e32 v42, v42, v0
	v_mul_f32_e32 v37, v37, v0
	v_mul_f32_e32 v34, v34, v0
	v_mul_f32_e32 v44, v44, v0
	v_mul_f32_e32 v43, v43, v0
	v_rndne_f32_e32 v45, v45
	v_rndne_f32_e32 v42, v42
	v_mul_f32_e32 v41, v41, v0
	v_mul_f32_e32 v38, v38, v0
	v_mul_f32_e32 v36, v36, v0
	v_mul_f32_e32 v35, v35, v0
	v_rndne_f32_e32 v37, v37
	v_rndne_f32_e32 v34, v34
	v_mul_f32_e32 v32, v32, v0
	v_mul_f32_e32 v33, v33, v0
	v_mul_f32_e32 v30, v30, v0
	v_rndne_f32_e32 v44, v44
	v_cvt_i32_f32_e32 v45, v45
	v_cvt_i32_f32_e32 v42, v42
	v_rndne_f32_e32 v43, v43
	v_mul_f32_e32 v40, v40, v0
	v_mul_f32_e32 v39, v39, v0
	v_rndne_f32_e32 v41, v41
	v_rndne_f32_e32 v38, v38
	v_rndne_f32_e32 v36, v36
	v_cvt_i32_f32_e32 v37, v37
	v_cvt_i32_f32_e32 v34, v34
	v_rndne_f32_e32 v35, v35
	v_mul_f32_e32 v0, v31, v0
	v_rndne_f32_e32 v31, v32
	v_rndne_f32_e32 v32, v33
	v_rndne_f32_e32 v30, v30
	v_cvt_i32_f32_e32 v44, v44
	v_cvt_i32_f32_e32 v43, v43
	v_rndne_f32_e32 v40, v40
	v_cvt_i32_f32_e32 v41, v41
	v_cvt_i32_f32_e32 v38, v38
	v_rndne_f32_e32 v39, v39
	v_cvt_i32_f32_e32 v36, v36
	v_cvt_i32_f32_e32 v35, v35
	v_cvt_i32_f32_e32 v32, v32
	v_cvt_i32_f32_e32 v30, v30
	v_rndne_f32_e32 v0, v0
	v_cvt_i32_f32_e32 v40, v40
	v_cvt_i32_f32_e32 v39, v39
	v_cvt_i32_f32_e32 v31, v31
	v_cvt_i32_f32_e32 v0, v0
	v_med3_i32 v45, v45, s84, v236
	v_med3_i32 v42, v42, s84, v236
	v_med3_i32 v37, v37, s84, v236
	v_med3_i32 v34, v34, s84, v236
	s_addc_u32 s13, s13, s43
	v_med3_i32 v44, v44, s84, v236
	v_med3_i32 v43, v43, s84, v236
	v_lshlrev_b32_e32 v45, 8, v45
	v_lshlrev_b32_e32 v42, 16, v42
	v_med3_i32 v41, v41, s84, v236
	v_med3_i32 v38, v38, s84, v236
	v_med3_i32 v36, v36, s84, v236
	v_med3_i32 v35, v35, s84, v236
	v_lshlrev_b32_e32 v37, 8, v37
	v_lshlrev_b32_e32 v34, 16, v34
	v_med3_i32 v32, v32, s84, v236
	v_med3_i32 v30, v30, s84, v236
	v_readlane_b32 s4, v254, 32
	v_lshlrev_b64 v[46:47], 10, v[46:47]
	v_and_b32_e32 v45, 0xff00, v45
	v_and_b32_e32 v42, 0xff0000, v42
	v_perm_b32 v43, v43, v44, s60
	v_med3_i32 v40, v40, s84, v236
	v_med3_i32 v39, v39, s84, v236
	v_lshlrev_b32_e32 v41, 8, v41
	v_lshlrev_b32_e32 v38, 16, v38
	v_and_b32_e32 v37, 0xff00, v37
	v_and_b32_e32 v34, 0xff0000, v34
	v_perm_b32 v35, v35, v36, s60
	v_med3_i32 v31, v31, s84, v236
	v_med3_i32 v0, v0, s84, v236
	v_lshlrev_b32_e32 v32, 8, v32
	v_lshlrev_b32_e32 v30, 16, v30
	v_readlane_b32 s5, v254, 33
	s_add_u32 s10, s10, s4
	v_or3_b32 v44, v43, v45, v42
	v_lshl_add_u64 v[42:43], v[18:19], 0, v[46:47]
	v_and_b32_e32 v41, 0xff00, v41
	v_and_b32_e32 v38, 0xff0000, v38
	v_perm_b32 v39, v39, v40, s60
	v_or3_b32 v34, v35, v37, v34
	v_and_b32_e32 v32, 0xff00, v32
	v_and_b32_e32 v30, 0xff0000, v30
	v_perm_b32 v0, v0, v31, s60
	s_addc_u32 s11, s11, s5
	v_or3_b32 v38, v39, v41, v38
	global_store_dword v[42:43], v34, off offset:512
	v_or3_b32 v0, v0, v32, v30
	v_lshl_add_u64 v[20:21], v[20:21], 0, s[78:79]
	s_cmpk_gt_i32 s12, 0x7fff
	s_waitcnt vmcnt(8)
	v_mov_b32_e32 v36, v22
	v_mov_b32_e32 v37, v23
	s_waitcnt vmcnt(7)
	v_mov_b32_e32 v34, v24
	v_mov_b32_e32 v35, v25
	s_waitcnt vmcnt(6)
	v_mov_b32_e32 v32, v26
	v_mov_b32_e32 v33, v27
	s_waitcnt vmcnt(5)
	v_mov_b32_e32 v30, v28
	v_mov_b32_e32 v31, v29
	global_store_dword v[42:43], v44, off
	global_store_dword v[42:43], v38, off offset:256
	global_store_dword v[42:43], v0, off offset:768
	s_cbranch_scc1 .LBB0_1024
.LBB0_1019:
	s_add_i32 s4, s42, s12
	s_cmpk_gt_i32 s4, 0x7fff
	s_cbranch_scc1 .LBB0_1021
	v_lshl_add_u64 v[22:23], s[6:7], 0, v[20:21]
	v_add_co_u32_e32 v28, vcc, 0x1c00000, v22
	s_nop 1
	v_addc_co_u32_e32 v29, vcc, 0, v23, vcc
	v_lshl_add_u64 v[64:65], v[28:29], 0, s[78:79]
	global_load_dwordx2 v[22:23], v[28:29], off
	global_load_dwordx2 v[24:25], v[28:29], off offset:512
	global_load_dwordx2 v[26:27], v[28:29], off offset:1024
	s_nop 0
	global_load_dwordx2 v[28:29], v[28:29], off offset:1536
	global_load_dwordx2 v[66:67], v[64:65], off
	global_load_dwordx2 v[66:67], v[64:65], off offset:512
	global_load_dwordx2 v[66:67], v[64:65], off offset:1024
	global_load_dwordx2 v[66:67], v[64:65], off offset:1536
	s_branch .LBB0_1022
